# baseline (speedup 1.0000x reference)
.LBB2_110:
.Lmk_gather:
	s_mov_b32 s30, s83
	v_lshl_or_b32 v10, v224, 7, v176
	s_cmp_lt_i32 s83, 9
	global_load_dwordx4 v[10:13], v10, s[28:29]
	s_cbranch_scc1 .LBB2_68
	v_lshl_or_b32 v14, v225, 7, v176
	s_cmp_lt_i32 s83, 17
	global_load_dwordx4 v[14:17], v14, s[28:29]
	s_cbranch_scc1 .LBB2_68
	v_lshl_or_b32 v30, v226, 7, v176
	s_cmp_lt_i32 s83, 25
	global_load_dwordx4 v[30:33], v30, s[28:29]
	s_cbranch_scc1 .LBB2_68
	v_lshl_or_b32 v26, v227, 7, v176
	s_cmp_lt_i32 s83, 33
	global_load_dwordx4 v[26:29], v26, s[28:29]
	s_cbranch_scc1 .LBB2_68
	v_lshl_or_b32 v2, v232, 7, v176
	s_cmp_lt_i32 s83, 41
	global_load_dwordx4 v[2:5], v2, s[28:29]
	s_cbranch_scc1 .LBB2_68
	v_lshl_or_b32 v6, v233, 7, v176
	s_cmp_lt_i32 s83, 49
	global_load_dwordx4 v[6:9], v6, s[28:29]
	s_cbranch_scc1 .LBB2_68
	v_lshl_or_b32 v18, v234, 7, v176
	s_cmp_lt_i32 s83, 57
	global_load_dwordx4 v[18:21], v18, s[28:29]
	s_cbranch_scc1 .LBB2_68
	v_lshl_or_b32 v22, v235, 7, v176
	global_load_dwordx4 v[22:25], v22, s[28:29]

.LBB2_72:
.LBB2_74:
	s_add_i32 s34, s45, -1
	s_cmp_lg_u32 s49, s34
	s_cbranch_scc1 .Lmk_tail
	s_and_b64 vcc, exec, s[54:55]
	s_cbranch_vccz .Lmk_ma_ready
	s_waitcnt vmcnt(1)
